# attention main loop: K/V LDS-DMA issued at the top of each step (slots free after the closing barrier), DMA addresses via SGPR base + 32-bit lane offsets, redundant max canonicalisations dropped
# speedup vs baseline: 1.0559x; 1.0100x over previous
.LBB0_724:
	v_lshlrev_b32_e32 v32, 1, v118
	v_and_b32_e32 v218, 32, v32
	v_lshrrev_b32_e32 v32, 2, v118
	v_and_or_b32 v32, v32, 3, v236
	v_lshlrev_b32_e32 v217, 6, v32
	v_add_u32_e32 v32, 0, v218
	v_add3_u32 v239, v32, v216, v217
	v_max3_f32 v32, v16, v17, v0
	v_max3_f32 v33, v18, v19, v1
	s_and_b32 s19, s41, 0x3fffffc0
	v_max3_f32 v32, v32, v2, v3
	v_max3_f32 v33, v33, v22, v23
	s_add_i32 s20, s45, 0x100
	v_max3_f32 v32, v32, v20, v21
	v_max3_f32 v33, v33, v6, v7
	s_lshl_b32 s19, s19, 2
	v_max3_f32 v32, v32, v4, v5
	v_max3_f32 v33, v33, v26, v27
	s_lshr_b32 s39, s20, 6
	v_max3_f32 v32, v32, v24, v25
	v_max3_f32 v33, v33, v10, v11
	s_mov_b64 s[20:21], 0x60000
	v_max3_f32 v32, v32, v8, v9
	v_max3_f32 v33, v33, v30, v31
	s_add_i32 s19, s19, 0
	v_max3_f32 v32, v32, v28, v29
	v_max3_f32 v33, v33, v14, v15
	s_cmp_lg_u32 0, -1
	v_max3_f32 v32, v32, v12, v13
	s_mov_b32 s96, 1
	v_max_f32_e32 v32, v32, v33
	s_mov_b32 s22, 0
	v_mov_b32_e32 v33, v32
	s_nop 1
	v_permlane32_swap_b32_e32 v32, v33
	v_max_f32_e32 v32, v32, v33
	v_lshl_add_u32 v235, v214, 2, s19
	v_sub_f32_e32 v64, v0, v32
	v_sub_f32_e32 v0, v17, v32
	v_sub_f32_e32 v16, v16, v32
	v_sub_f32_e32 v65, v1, v32
	v_sub_f32_e32 v1, v18, v32
	v_sub_f32_e32 v66, v2, v32
	v_sub_f32_e32 v2, v19, v32
	s_nop 0
	v_exp_f32_e32 v81, v0
	v_lshl_add_u32 v0, v236, 2, 0
	v_sub_f32_e32 v67, v3, v32
	v_sub_f32_e32 v3, v20, v32
	v_sub_f32_e32 v68, v4, v32
	v_sub_f32_e32 v4, v21, v32
	v_sub_f32_e32 v69, v5, v32
	v_sub_f32_e32 v5, v22, v32
	v_sub_f32_e32 v70, v6, v32
	v_sub_f32_e32 v6, v23, v32
	v_sub_f32_e32 v71, v7, v32
	v_sub_f32_e32 v7, v24, v32
	v_sub_f32_e32 v72, v8, v32
	v_sub_f32_e32 v8, v25, v32
	v_sub_f32_e32 v73, v9, v32
	v_sub_f32_e32 v9, v26, v32
	v_sub_f32_e32 v74, v10, v32
	v_sub_f32_e32 v10, v27, v32
	v_sub_f32_e32 v75, v11, v32
	v_sub_f32_e32 v11, v28, v32
	v_sub_f32_e32 v76, v12, v32
	v_sub_f32_e32 v12, v29, v32
	v_sub_f32_e32 v77, v13, v32
	v_sub_f32_e32 v13, v30, v32
	v_sub_f32_e32 v78, v14, v32
	v_sub_f32_e32 v14, v31, v32
	v_add_u32_e32 v28, 0x15100, v0
	v_sub_f32_e32 v79, v15, v32
	v_exp_f32_e32 v80, v16
	v_exp_f32_e32 v82, v1
	v_exp_f32_e32 v83, v2
	v_exp_f32_e32 v84, v3
	v_exp_f32_e32 v85, v4
	v_exp_f32_e32 v86, v5
	v_exp_f32_e32 v87, v6
	v_exp_f32_e32 v88, v7
	v_exp_f32_e32 v89, v8
	v_exp_f32_e32 v90, v9
	v_exp_f32_e32 v91, v10
	v_exp_f32_e32 v92, v11
	v_exp_f32_e32 v93, v12
	v_exp_f32_e32 v94, v13
	v_exp_f32_e32 v95, v14
	ds_read_b128 v[0:3], v28
	ds_read_b128 v[4:7], v28 offset:32
	ds_read_b128 v[8:11], v28 offset:128
	ds_read_b128 v[12:15], v28 offset:160
	ds_read_b128 v[16:19], v28 offset:64
	ds_read_b128 v[20:23], v28 offset:96
	ds_read_b128 v[24:27], v28 offset:192
	ds_read_b128 v[28:31], v28 offset:224
	s_waitcnt vmcnt(0) lgkmcnt(0)
	s_barrier
	v_add_f32_e32 v202, v97, v32
	v_exp_f32_e32 v64, v64
	s_waitcnt lgkmcnt(7)
	v_pk_add_f32 v[48:49], v[202:203], v[0:1] op_sel_hi:[0,1] neg_lo:[1,0] neg_hi:[1,0]
	v_lshl_add_u64 v[0:1], v[114:115], 0, s[20:21]
	s_mov_b32 s20, m0
	s_mov_b32 m0, s30
	s_nop 0
	global_load_lds_dwordx4 v[0:1], off
	s_mov_b32 m0, s20
	s_mov_b64 s[20:21], 0x20000
	v_lshl_add_u64 v[0:1], v[116:117], 0, s[20:21]
	s_cselect_b32 s20, 0, 0
	s_add_i32 s18, s20, s18
	s_add_i32 s18, s18, 0x8000
	s_mov_b32 s20, m0
	s_mov_b32 m0, s18
	s_nop 0
	global_load_lds_dwordx4 v[0:1], off
	s_mov_b32 m0, s20
	ds_read_b128 v[158:161], v238 offset:8192
	ds_read_b128 v[146:149], v238 offset:8704
	ds_read_b128 v[154:157], v238 offset:10240
	ds_read_b128 v[142:145], v238 offset:10752
	ds_read_b128 v[150:153], v238 offset:12288
	ds_read_b128 v[138:141], v238 offset:12800
	ds_read_b128 v[134:137], v238 offset:14336
	ds_read_b128 v[130:133], v238 offset:14848
	v_exp_f32_e32 v65, v65
	v_exp_f32_e32 v66, v66
	v_exp_f32_e32 v67, v67
	v_exp_f32_e32 v68, v68
	v_exp_f32_e32 v69, v69
	v_exp_f32_e32 v70, v70
	v_exp_f32_e32 v71, v71
	v_exp_f32_e32 v72, v72
	v_exp_f32_e32 v73, v73
	v_exp_f32_e32 v74, v74
	v_exp_f32_e32 v75, v75
	v_exp_f32_e32 v76, v76
	v_exp_f32_e32 v77, v77
	v_exp_f32_e32 v78, v78
	v_exp_f32_e32 v79, v79
	s_waitcnt vmcnt(2) lgkmcnt(0)
	s_barrier
	v_and_b32_e32 v0, 3, v118
	s_waitcnt lgkmcnt(13)
	v_pk_add_f32 v[32:33], v[202:203], v[8:9] op_sel_hi:[0,1] neg_lo:[1,0] neg_hi:[1,0]
	v_pk_add_f32 v[50:51], v[202:203], v[2:3] op_sel_hi:[0,1] neg_lo:[1,0] neg_hi:[1,0]
	v_pk_add_f32 v[34:35], v[202:203], v[10:11] op_sel_hi:[0,1] neg_lo:[1,0] neg_hi:[1,0]
	v_pk_add_f32 v[52:53], v[202:203], v[4:5] op_sel_hi:[0,1] neg_lo:[1,0] neg_hi:[1,0]
	s_waitcnt lgkmcnt(12)
	v_pk_add_f32 v[36:37], v[202:203], v[12:13] op_sel_hi:[0,1] neg_lo:[1,0] neg_hi:[1,0]
	v_pk_add_f32 v[54:55], v[202:203], v[6:7] op_sel_hi:[0,1] neg_lo:[1,0] neg_hi:[1,0]
	v_pk_add_f32 v[38:39], v[202:203], v[14:15] op_sel_hi:[0,1] neg_lo:[1,0] neg_hi:[1,0]
	s_waitcnt lgkmcnt(11)
	v_pk_add_f32 v[56:57], v[202:203], v[16:17] op_sel_hi:[0,1] neg_lo:[1,0] neg_hi:[1,0]
	s_waitcnt lgkmcnt(9)
	v_pk_add_f32 v[40:41], v[202:203], v[24:25] op_sel_hi:[0,1] neg_lo:[1,0] neg_hi:[1,0]
	v_pk_add_f32 v[58:59], v[202:203], v[18:19] op_sel_hi:[0,1] neg_lo:[1,0] neg_hi:[1,0]
	v_pk_add_f32 v[42:43], v[202:203], v[26:27] op_sel_hi:[0,1] neg_lo:[1,0] neg_hi:[1,0]
	v_pk_add_f32 v[60:61], v[202:203], v[20:21] op_sel_hi:[0,1] neg_lo:[1,0] neg_hi:[1,0]
	s_waitcnt lgkmcnt(8)
	v_pk_add_f32 v[44:45], v[202:203], v[28:29] op_sel_hi:[0,1] neg_lo:[1,0] neg_hi:[1,0]
	v_pk_add_f32 v[62:63], v[202:203], v[22:23] op_sel_hi:[0,1] neg_lo:[1,0] neg_hi:[1,0]
	v_pk_add_f32 v[46:47], v[202:203], v[30:31] op_sel_hi:[0,1] neg_lo:[1,0] neg_hi:[1,0]
	s_andn2_b64 vcc, exec, s[2:3]
	v_cmp_gt_u32_e64 s[2:3], 32, v199
	v_lshl_add_u32 v219, v236, 2, s19
	v_lshlrev_b32_e32 v204, 4, v0
	s_cbranch_vccnz .LBB0_742
	s_lshl_b64 s[18:19], s[4:5], 1
	s_add_u32 s18, s70, s18
	s_addc_u32 s19, s71, s19
	s_add_u32 s18, s18, s14
	s_addc_u32 s19, s19, s15
	v_lshl_add_u64 v[206:207], s[18:19], 0, v[96:97]
	s_lshl_b64 s[18:19], s[16:17], 1
	s_add_u32 s18, s18, s14
	v_mov_b32_e32 v205, v97
	s_addc_u32 s19, s19, s15
	v_lshl_add_u64 v[0:1], s[18:19], 0, v[204:205]
	s_lshl_b32 s18, s41, 9
	s_and_b32 s18, s18, 0x18000
	v_lshl_or_b32 v2, v241, 11, s18
	v_mov_b32_e32 v3, v97
	v_lshl_add_u64 v[0:1], v[0:1], 0, v[2:3]
	v_mov_b32_e32 v16, v97
	v_mov_b32_e32 v17, v97
	v_lshl_add_u64 v[208:209], s[70:71], 0, v[0:1]
	v_subrev_u32_e32 v245, s14, v0
	v_add_u32_e32 v245, 0x7fc0000, v245
	v_lshl_add_u32 v244, s4, 1, v96
	s_add_u32 s98, s70, s14
	s_addc_u32 s99, s71, s15
	s_add_u32 s98, s98, s12
	s_addc_u32 s99, s99, s13
	s_add_u32 s98, s98, 0x16e80000
	s_addc_u32 s99, s99, 0
	v_readlane_b32 s18, v253, 11
	v_mov_b32_e32 v18, v97
	v_mov_b32_e32 v19, v97
	v_mov_b32_e32 v20, v97
	v_mov_b32_e32 v21, v97
	v_mov_b32_e32 v22, v97
	v_mov_b32_e32 v23, v97
	v_mov_b32_e32 v24, v97
	v_mov_b32_e32 v25, v97
	v_mov_b32_e32 v26, v97
	v_mov_b32_e32 v27, v97
	v_mov_b32_e32 v28, v97
	v_mov_b32_e32 v29, v97
	v_mov_b32_e32 v30, v97
	v_mov_b32_e32 v31, v97
	v_mov_b64_e32 v[0:1], v[16:17]
	v_lshl_add_u32 v205, v215, 4, s18
	s_mov_b32 s18, 0
	s_movk_i32 s22, 0x4000
	s_movk_i32 s38, 0x2000
	v_mov_b32_e32 v240, 0
	s_mov_b32 s23, 6
	v_mov_b64_e32 v[2:3], v[18:19]
	v_mov_b64_e32 v[4:5], v[20:21]
	v_mov_b64_e32 v[6:7], v[22:23]
	v_mov_b64_e32 v[8:9], v[24:25]
	v_mov_b64_e32 v[10:11], v[26:27]
	v_mov_b64_e32 v[12:13], v[28:29]
	v_mov_b64_e32 v[14:15], v[30:31]
.LBB0_726:
	v_add_u32_e32 v164, s18, v239
	s_add_i32 s18, s38, s30
	s_mov_b32 s19, m0
	s_mov_b32 m0, s18
	s_nop 0
	global_load_lds_dwordx4 v244, s[98:99]
	s_mov_b32 m0, s19
	s_add_i32 s18, s22, s31
	s_mov_b32 s19, m0
	s_mov_b32 m0, s18
	s_nop 0
	global_load_lds_dwordx4 v245, s[98:99]
	s_mov_b32 m0, s19
	s_add_u32 s98, s98, 0x20000
	s_addc_u32 s99, s99, 0
	ds_read_b64_tr_b16 v[190:191], v164 offset:24576
	ds_read_b64_tr_b16 v[192:193], v164 offset:25088
	s_waitcnt lgkmcnt(2)
	v_mfma_f32_32x32x16_bf16 v[48:63], v[158:161], v[110:113], v[48:63]
	v_add_f32_e32 v114, v80, v81
	v_add_f32_e32 v114, v82, v114
	v_add_f32_e32 v114, v83, v114
	v_add_f32_e32 v114, v84, v114
	v_add_f32_e32 v114, v85, v114
	v_cvt_pk_bf16_f32 v126, v80, v81
	v_cvt_pk_bf16_f32 v127, v82, v83
	ds_read_b64_tr_b16 v[186:187], v164 offset:28672
	ds_read_b64_tr_b16 v[188:189], v164 offset:29184
	v_mfma_f32_32x32x16_bf16 v[32:47], v[146:149], v[110:113], v[32:47]
	v_add_f32_e32 v80, v86, v114
	v_add_f32_e32 v80, v87, v80
	v_add_f32_e32 v80, v88, v80
	v_add_f32_e32 v80, v89, v80
	v_cvt_pk_bf16_f32 v128, v84, v85
	v_cvt_pk_bf16_f32 v129, v86, v87
	ds_read_b64_tr_b16 v[182:183], v164 offset:25600
	ds_read_b64_tr_b16 v[184:185], v164 offset:26112
	v_mfma_f32_32x32x16_bf16 v[48:63], v[154:157], v[106:109], v[48:63]
	v_add_f32_e32 v80, v90, v80
	v_add_f32_e32 v80, v91, v80
	v_add_f32_e32 v80, v92, v80
	v_add_f32_e32 v80, v93, v80
	v_cvt_pk_bf16_f32 v122, v88, v89
	v_cvt_pk_bf16_f32 v123, v90, v91
	ds_read_b64_tr_b16 v[178:179], v164 offset:29696
	ds_read_b64_tr_b16 v[180:181], v164 offset:30208
	v_mfma_f32_32x32x16_bf16 v[32:47], v[142:145], v[106:109], v[32:47]
	v_add_f32_e32 v80, v94, v80
	v_add_f32_e32 v80, v95, v80
	v_add_f32_e32 v80, v64, v80
	v_add_f32_e32 v80, v65, v80
	v_cvt_pk_bf16_f32 v124, v92, v93
	v_cvt_pk_bf16_f32 v125, v94, v95
	ds_read_b64_tr_b16 v[166:167], v164 offset:26624
	ds_read_b64_tr_b16 v[168:169], v164 offset:27136
	v_mfma_f32_32x32x16_bf16 v[48:63], v[150:153], v[102:105], v[48:63]
	v_add_f32_e32 v80, v66, v80
	v_add_f32_e32 v80, v67, v80
	v_add_f32_e32 v80, v68, v80
	v_add_f32_e32 v80, v69, v80
	v_cvt_pk_bf16_f32 v118, v64, v65
	v_cvt_pk_bf16_f32 v119, v66, v67
	ds_read_b64_tr_b16 v[174:175], v164 offset:30720
	ds_read_b64_tr_b16 v[176:177], v164 offset:31232
	v_mfma_f32_32x32x16_bf16 v[32:47], v[138:141], v[102:105], v[32:47]
	v_add_f32_e32 v64, v70, v80
	v_add_f32_e32 v64, v71, v64
	v_add_f32_e32 v64, v72, v64
	v_add_f32_e32 v64, v73, v64
	v_cvt_pk_bf16_f32 v120, v68, v69
	v_cvt_pk_bf16_f32 v121, v70, v71
	ds_read_b64_tr_b16 v[170:171], v164 offset:27648
	ds_read_b64_tr_b16 v[172:173], v164 offset:28160
	v_mfma_f32_32x32x16_bf16 v[48:63], v[134:137], v[98:101], v[48:63]
	v_add_f32_e32 v64, v74, v64
	v_add_f32_e32 v64, v75, v64
	v_add_f32_e32 v64, v76, v64
	v_add_f32_e32 v64, v77, v64
	v_cvt_pk_bf16_f32 v114, v72, v73
	v_cvt_pk_bf16_f32 v115, v74, v75
	ds_read_b64_tr_b16 v[162:163], v164 offset:31744
	ds_read_b64_tr_b16 v[164:165], v164 offset:32256
	v_mfma_f32_32x32x16_bf16 v[32:47], v[130:133], v[98:101], v[32:47]
	v_add_f32_e32 v64, v78, v64
	v_add_f32_e32 v64, v79, v64
	v_add_f32_e32 v224, v240, v64
	v_cvt_pk_bf16_f32 v116, v76, v77
	v_cvt_pk_bf16_f32 v117, v78, v79
	s_waitcnt lgkmcnt(14)
	ds_read_b128 v[64:67], v205
	ds_read_b128 v[68:71], v205 offset:32
	ds_read_b128 v[82:85], v205 offset:128
	ds_read_b128 v[86:89], v205 offset:160
	ds_read_b128 v[72:75], v205 offset:64
	ds_read_b128 v[76:79], v205 offset:96
	ds_read_b128 v[90:93], v205 offset:192
	ds_read_b128 v[138:141], v205 offset:224
	v_max_f32_e32 v80, v48, v49
	v_max3_f32 v81, v50, v51, v33
	v_max3_f32 v80, v80, v32, v34
	v_max3_f32 v80, v80, v35, v52
	v_max3_f32 v81, v81, v54, v55
	v_max3_f32 v80, v80, v53, v36
	v_max3_f32 v81, v81, v38, v39
	v_max3_f32 v80, v80, v37, v56
	v_max3_f32 v81, v81, v58, v59
	v_max3_f32 v80, v80, v57, v40
	v_max3_f32 v81, v81, v42, v43
	v_max3_f32 v80, v80, v41, v60
	v_max3_f32 v81, v81, v62, v63
	v_max3_f32 v80, v80, v61, v44
	v_max3_f32 v81, v81, v46, v47
	v_max3_f32 v80, v80, v45, v81
	v_mov_b32_e32 v81, v80
	s_nop 1
	v_permlane32_swap_b32_e32 v80, v81
	v_max_f32_e32 v80, v80, v81
	v_cmp_lt_f32_e32 vcc, s51, v80
	s_cmp_lg_u64 vcc, 0
	s_cselect_b64 s[18:19], -1, 0
	s_cbranch_vccnz .LBB0_734

.LBB0_729:
	v_pk_add_f32 v[80:81], v[64:65], v[202:203] op_sel_hi:[1,0] neg_lo:[0,1] neg_hi:[0,1]
	s_waitcnt lgkmcnt(13)
	v_pk_add_f32 v[64:65], v[82:83], v[202:203] op_sel_hi:[1,0] neg_lo:[0,1] neg_hi:[0,1]
	v_pk_add_f32 v[82:83], v[66:67], v[202:203] op_sel_hi:[1,0] neg_lo:[0,1] neg_hi:[0,1]
	v_pk_add_f32 v[66:67], v[84:85], v[202:203] op_sel_hi:[1,0] neg_lo:[0,1] neg_hi:[0,1]
	v_pk_add_f32 v[84:85], v[68:69], v[202:203] op_sel_hi:[1,0] neg_lo:[0,1] neg_hi:[0,1]
	s_waitcnt lgkmcnt(12)
	v_pk_add_f32 v[68:69], v[86:87], v[202:203] op_sel_hi:[1,0] neg_lo:[0,1] neg_hi:[0,1]
	v_pk_add_f32 v[86:87], v[70:71], v[202:203] op_sel_hi:[1,0] neg_lo:[0,1] neg_hi:[0,1]
	v_pk_add_f32 v[70:71], v[88:89], v[202:203] op_sel_hi:[1,0] neg_lo:[0,1] neg_hi:[0,1]
	s_waitcnt lgkmcnt(11)
	v_pk_add_f32 v[88:89], v[72:73], v[202:203] op_sel_hi:[1,0] neg_lo:[0,1] neg_hi:[0,1]
	s_waitcnt lgkmcnt(9)
	v_pk_add_f32 v[72:73], v[90:91], v[202:203] op_sel_hi:[1,0] neg_lo:[0,1] neg_hi:[0,1]
	v_pk_add_f32 v[90:91], v[74:75], v[202:203] op_sel_hi:[1,0] neg_lo:[0,1] neg_hi:[0,1]
	v_pk_add_f32 v[74:75], v[92:93], v[202:203] op_sel_hi:[1,0] neg_lo:[0,1] neg_hi:[0,1]
	v_pk_add_f32 v[92:93], v[76:77], v[202:203] op_sel_hi:[1,0] neg_lo:[0,1] neg_hi:[0,1]
	s_waitcnt lgkmcnt(8)
	v_pk_add_f32 v[76:77], v[138:139], v[202:203] op_sel_hi:[1,0] neg_lo:[0,1] neg_hi:[0,1]
	v_pk_add_f32 v[94:95], v[78:79], v[202:203] op_sel_hi:[1,0] neg_lo:[0,1] neg_hi:[0,1]
	v_pk_add_f32 v[78:79], v[140:141], v[202:203] op_sel_hi:[1,0] neg_lo:[0,1] neg_hi:[0,1]
	s_add_i32 s18, s22, 0x2000
	v_add_u32_e32 v162, s38, v239
	s_cmpk_lg_i32 s22, 0x4000
	s_cselect_b32 s38, s18, 0
	s_add_i32 s18, s22, s30
	s_mov_b32 s19, m0
	s_mov_b32 m0, s18
	s_nop 0
	global_load_lds_dwordx4 v244, s[98:99]
	s_mov_b32 m0, s19
	s_add_i32 s18, s38, s31
	s_mov_b32 s19, m0
	s_mov_b32 m0, s18
	s_nop 0
	global_load_lds_dwordx4 v245, s[98:99]
	s_mov_b32 m0, s19
	s_add_u32 s98, s98, 0x20000
	s_addc_u32 s99, s99, 0
	ds_read_b64_tr_b16 v[194:195], v162 offset:24576
	ds_read_b64_tr_b16 v[196:197], v162 offset:25088
	s_waitcnt lgkmcnt(2)
	v_mfma_f32_32x32x16_bf16 v[80:95], v[134:137], v[110:113], v[80:95]
	v_add_f32_e32 v114, v48, v49
	v_add_f32_e32 v114, v50, v114
	v_add_f32_e32 v114, v51, v114
	v_add_f32_e32 v114, v52, v114
	v_add_f32_e32 v114, v53, v114
	v_cvt_pk_bf16_f32 v126, v48, v49
	v_cvt_pk_bf16_f32 v127, v50, v51
	ds_read_b64_tr_b16 v[190:191], v162 offset:28672
	ds_read_b64_tr_b16 v[192:193], v162 offset:29184
	v_mfma_f32_32x32x16_bf16 v[64:79], v[130:133], v[110:113], v[64:79]
	v_add_f32_e32 v48, v54, v114
	v_add_f32_e32 v48, v55, v48
	v_add_f32_e32 v48, v56, v48
	v_add_f32_e32 v48, v57, v48
	v_cvt_pk_bf16_f32 v128, v52, v53
	v_cvt_pk_bf16_f32 v129, v54, v55
	ds_read_b64_tr_b16 v[186:187], v162 offset:25600
	ds_read_b64_tr_b16 v[188:189], v162 offset:26112
	v_mfma_f32_32x32x16_bf16 v[80:95], v[146:149], v[106:109], v[80:95]
	v_add_f32_e32 v48, v58, v48
	v_add_f32_e32 v48, v59, v48
	v_add_f32_e32 v48, v60, v48
	v_add_f32_e32 v48, v61, v48
	v_cvt_pk_bf16_f32 v122, v56, v57
	v_cvt_pk_bf16_f32 v123, v58, v59
	ds_read_b64_tr_b16 v[138:139], v162 offset:29696
	ds_read_b64_tr_b16 v[140:141], v162 offset:30208
	v_mfma_f32_32x32x16_bf16 v[64:79], v[142:145], v[106:109], v[64:79]
	v_add_f32_e32 v48, v62, v48
	v_add_f32_e32 v48, v63, v48
	v_add_f32_e32 v48, v32, v48
	v_add_f32_e32 v48, v33, v48
	v_cvt_pk_bf16_f32 v124, v60, v61
	v_cvt_pk_bf16_f32 v125, v62, v63
	ds_read_b64_tr_b16 v[182:183], v162 offset:26624
	ds_read_b64_tr_b16 v[184:185], v162 offset:27136
	v_mfma_f32_32x32x16_bf16 v[80:95], v[158:161], v[102:105], v[80:95]
	v_add_f32_e32 v48, v34, v48
	v_add_f32_e32 v48, v35, v48
	v_add_f32_e32 v48, v36, v48
	v_add_f32_e32 v48, v37, v48
	v_cvt_pk_bf16_f32 v118, v32, v33
	v_cvt_pk_bf16_f32 v119, v34, v35
	ds_read_b64_tr_b16 v[178:179], v162 offset:30720
	ds_read_b64_tr_b16 v[180:181], v162 offset:31232
	v_mfma_f32_32x32x16_bf16 v[64:79], v[154:157], v[102:105], v[64:79]
	v_add_f32_e32 v32, v38, v48
	v_add_f32_e32 v32, v39, v32
	v_add_f32_e32 v32, v40, v32
	v_add_f32_e32 v32, v41, v32
	v_cvt_pk_bf16_f32 v120, v36, v37
	v_cvt_pk_bf16_f32 v121, v38, v39
	ds_read_b64_tr_b16 v[174:175], v162 offset:27648
	ds_read_b64_tr_b16 v[176:177], v162 offset:28160
	v_mfma_f32_32x32x16_bf16 v[80:95], v[166:169], v[98:101], v[80:95]
	v_add_f32_e32 v32, v42, v32
	v_add_f32_e32 v32, v43, v32
	v_add_f32_e32 v32, v44, v32
	v_add_f32_e32 v32, v45, v32
	v_cvt_pk_bf16_f32 v114, v40, v41
	v_cvt_pk_bf16_f32 v115, v42, v43
	ds_read_b64_tr_b16 v[170:171], v162 offset:31744
	ds_read_b64_tr_b16 v[172:173], v162 offset:32256
	v_mfma_f32_32x32x16_bf16 v[64:79], v[150:153], v[98:101], v[64:79]
	v_add_f32_e32 v32, v46, v32
	v_add_f32_e32 v32, v47, v32
	v_add_f32_e32 v240, v224, v32
	v_cvt_pk_bf16_f32 v116, v44, v45
	v_cvt_pk_bf16_f32 v117, v46, v47
	s_waitcnt lgkmcnt(14)
	ds_read_b128 v[32:35], v205 offset:256
	ds_read_b128 v[36:39], v205 offset:288
	ds_read_b128 v[50:53], v205 offset:384
	ds_read_b128 v[54:57], v205 offset:416
	ds_read_b128 v[40:43], v205 offset:320
	ds_read_b128 v[44:47], v205 offset:352
	ds_read_b128 v[58:61], v205 offset:448
	ds_read_b128 v[162:165], v205 offset:480
	v_max_f32_e32 v48, v80, v81
	v_max3_f32 v49, v82, v83, v65
	v_max3_f32 v48, v48, v64, v66
	v_max3_f32 v48, v48, v67, v84
	v_max3_f32 v49, v49, v86, v87
	v_max3_f32 v48, v48, v85, v68
	v_max3_f32 v49, v49, v70, v71
	v_max3_f32 v48, v48, v69, v88
	v_max3_f32 v49, v49, v90, v91
	v_max3_f32 v48, v48, v89, v72
	v_max3_f32 v49, v49, v74, v75
	v_max3_f32 v48, v48, v73, v92
	v_max3_f32 v49, v49, v94, v95
	v_max3_f32 v48, v48, v93, v76
	v_max3_f32 v49, v49, v78, v79
	v_max3_f32 v48, v48, v77, v49
	v_mov_b32_e32 v49, v48
	s_nop 1
	v_permlane32_swap_b32_e32 v48, v49
	v_max_f32_e32 v48, v48, v49
	v_cmp_lt_f32_e32 vcc, s51, v48
	s_cmp_lg_u64 vcc, 0
	s_cselect_b64 s[18:19], -1, 0
	s_cbranch_vccnz .LBB0_737
